# static s_setprio 1 for waves 0-3 instead (mirror of the previous version), flips deleted
# baseline (speedup 1.0000x reference)
.LBB2_32:
	s_xor_b64 s[30:31], s[4:5], -1
	s_lshl_b32 s4, s63, 8
	s_ashr_i32 s5, s4, 31
	s_lshl_b64 s[4:5], s[4:5], 11
	s_add_u32 s4, s14, s4
	s_addc_u32 s5, s15, s5
	s_add_u32 s24, s4, 0x400000
	s_addc_u32 s25, s5, 0
	s_and_b64 s[4:5], s[28:29], exec
	s_cselect_b32 s66, s25, s19
	s_cselect_b32 s67, s24, s18
	s_lshl_b32 s4, s62, 8
	s_ashr_i32 s5, s4, 31
	s_lshl_b64 s[4:5], s[4:5], 11
	s_add_u32 s26, s12, s4
	s_addc_u32 s27, s13, s5
	s_and_b64 s[4:5], s[28:29], exec
	s_cselect_b32 s68, s27, s1
	s_cselect_b32 s69, s26, s0
	s_add_u32 s70, s18, 0x40080
	s_addc_u32 s71, s19, 0
	s_add_u32 s72, s0, 0x100
	v_mov_b64_e32 v[0:1], 0
	s_addc_u32 s73, s1, 0
	s_mov_b32 s74, -2
	v_mov_b64_e32 v[2:3], 0
	v_mov_b64_e32 v[4:5], 0
	v_mov_b64_e32 v[6:7], 0
	v_mov_b64_e32 v[8:9], 0
	v_mov_b64_e32 v[10:11], 0
	v_mov_b64_e32 v[12:13], 0
	v_mov_b64_e32 v[14:15], 0
	v_mov_b64_e32 v[16:17], 0
	v_mov_b64_e32 v[18:19], 0
	v_mov_b64_e32 v[20:21], 0
	v_mov_b64_e32 v[22:23], 0
	v_mov_b64_e32 v[24:25], 0
	v_mov_b64_e32 v[26:27], 0
	v_mov_b64_e32 v[28:29], 0
	v_mov_b64_e32 v[30:31], 0
	v_mov_b64_e32 v[32:33], 0
	v_mov_b64_e32 v[34:35], 0
	v_mov_b64_e32 v[36:37], 0
	v_mov_b64_e32 v[38:39], 0
	v_mov_b64_e32 v[40:41], 0
	v_mov_b64_e32 v[42:43], 0
	v_mov_b64_e32 v[44:45], 0
	v_mov_b64_e32 v[46:47], 0
	v_mov_b64_e32 v[48:49], 0
	v_mov_b64_e32 v[50:51], 0
	v_mov_b64_e32 v[52:53], 0
	v_mov_b64_e32 v[54:55], 0
	v_mov_b64_e32 v[56:57], 0
	v_mov_b64_e32 v[58:59], 0
	v_mov_b64_e32 v[60:61], 0
	v_mov_b64_e32 v[62:63], 0
	v_mov_b64_e32 v[64:65], 0
	v_mov_b64_e32 v[66:67], 0
	v_mov_b64_e32 v[68:69], 0
	v_mov_b64_e32 v[70:71], 0
	v_mov_b64_e32 v[72:73], 0
	v_mov_b64_e32 v[74:75], 0
	v_mov_b64_e32 v[76:77], 0
	v_mov_b64_e32 v[78:79], 0
	v_mov_b64_e32 v[80:81], 0
	v_mov_b64_e32 v[82:83], 0
	v_mov_b64_e32 v[84:85], 0
	v_mov_b64_e32 v[86:87], 0
	v_mov_b64_e32 v[88:89], 0
	v_mov_b64_e32 v[90:91], 0
	v_mov_b64_e32 v[92:93], 0
	v_mov_b64_e32 v[94:95], 0
	v_mov_b64_e32 v[96:97], 0
	v_mov_b64_e32 v[98:99], 0
	v_mov_b64_e32 v[100:101], 0
	v_mov_b64_e32 v[102:103], 0
	v_mov_b64_e32 v[104:105], 0
	v_mov_b64_e32 v[106:107], 0
	v_mov_b64_e32 v[108:109], 0
	v_mov_b64_e32 v[110:111], 0
	v_mov_b64_e32 v[112:113], 0
	v_mov_b64_e32 v[114:115], 0
	v_mov_b64_e32 v[116:117], 0
	v_mov_b64_e32 v[118:119], 0
	v_mov_b64_e32 v[120:121], 0
	v_mov_b64_e32 v[122:123], 0
	v_mov_b64_e32 v[124:125], 0
	v_mov_b64_e32 v[126:127], 0
	s_waitcnt lgkmcnt(0)
	v_add_u32_e32 v212, 0x1c000, v199
	v_add_u32_e32 v213, 0x1c000, v200
	s_cmpk_lt_u32 s33, 0x100
	s_cbranch_scc0 .Lp1_prio_done
	s_setprio 1

.Lp2_sum_skip:
	s_barrier
	buffer_load_dwordx4 v194, s[12:15], 0 offen lds
	s_mov_b32 m0, s41
	v_lshrrev_b32_e32 v2, 4, v0
	buffer_load_dwordx4 v196, s[12:15], 0 offen lds
	s_add_u32 s12, s16, 0x80
	s_addc_u32 s0, s9, 0
	s_add_i32 s42, s31, 0x8000
	s_and_b32 s13, s0, 0xffff
	s_mov_b32 m0, s42
	s_add_i32 s43, s31, 0xa000
	buffer_load_dwordx4 v1, s[12:15], 0 offen lds
	s_mov_b32 m0, s43
	v_and_b32_e32 v197, 15, v0
	buffer_load_dwordx4 v195, s[12:15], 0 offen lds
	s_add_u32 s12, s8, 0x10080
	s_addc_u32 s0, s25, 0
	s_add_i32 s44, s31, 0x1c000
	s_and_b32 s13, s0, 0xffff
	s_mov_b32 m0, s44
	s_add_i32 s45, s31, 0x1e000
	buffer_load_dwordx4 v194, s[12:15], 0 offen lds
	s_mov_b32 m0, s45
	s_and_b32 s0, s2, 1
	buffer_load_dwordx4 v196, s[12:15], 0 offen lds
	s_lshl_b32 s0, s0, 23
	s_lshl_b32 s1, s26, 21
	v_bfe_u32 v3, v0, 1, 3
	s_or_b32 s0, s0, s1
	v_bitop3_b32 v2, v2, v3, 3 bitop3:0x6c
	v_lshlrev_b32_e32 v3, 7, v197
	s_add_i32 s46, s31, 0xc000
	s_add_i32 s47, s31, 0xe000
	s_or_b32 s0, s27, s0
	v_lshlrev_b32_e32 v2, 4, v2
	v_lshl_or_b32 v4, s28, 13, v3
	v_lshl_or_b32 v3, s39, 12, v3
	s_waitcnt vmcnt(6)
	s_add_u32 s48, s20, s0
	v_or_b32_e32 v5, v4, v2
	v_bitop3_b32 v4, v4, 64, v2 bitop3:0x36
	v_or_b32_e32 v198, v3, v2
	v_bitop3_b32 v199, v3, 64, v2 bitop3:0x36
	s_addc_u32 s49, s21, 0
	v_mov_b32_e32 v66, 0
	s_add_i32 s0, 0, 0x10000
	s_add_i32 s1, 0, 0x14000
	s_mov_b32 s50, -2
	s_mov_b64 s[10:11], 0
	v_add_u32_e32 v200, 0, v5
	v_add_u32_e32 v201, 0, v4
	v_mov_b32_e32 v67, v66
	v_mov_b32_e32 v68, v66
	v_mov_b32_e32 v69, v66
	v_mov_b32_e32 v70, v66
	v_mov_b32_e32 v71, v66
	v_mov_b32_e32 v72, v66
	v_mov_b32_e32 v73, v66
	v_mov_b32_e32 v82, v66
	v_mov_b32_e32 v83, v66
	v_mov_b32_e32 v84, v66
	v_mov_b32_e32 v85, v66
	v_mov_b32_e32 v86, v66
	v_mov_b32_e32 v87, v66
	v_mov_b32_e32 v88, v66
	v_mov_b32_e32 v89, v66
	v_mov_b32_e32 v98, v66
	v_mov_b32_e32 v99, v66
	v_mov_b32_e32 v100, v66
	v_mov_b32_e32 v101, v66
	v_mov_b32_e32 v102, v66
	v_mov_b32_e32 v103, v66
	v_mov_b32_e32 v104, v66
	v_mov_b32_e32 v105, v66
	v_mov_b32_e32 v114, v66
	v_mov_b32_e32 v115, v66
	v_mov_b32_e32 v116, v66
	v_mov_b32_e32 v117, v66
	v_mov_b32_e32 v118, v66
	v_mov_b32_e32 v119, v66
	v_mov_b32_e32 v120, v66
	v_mov_b32_e32 v121, v66
	v_mov_b32_e32 v74, v66
	v_mov_b32_e32 v75, v66
	v_mov_b32_e32 v76, v66
	v_mov_b32_e32 v77, v66
	v_mov_b32_e32 v78, v66
	v_mov_b32_e32 v79, v66
	v_mov_b32_e32 v80, v66
	v_mov_b32_e32 v81, v66
	v_mov_b32_e32 v90, v66
	v_mov_b32_e32 v91, v66
	v_mov_b32_e32 v92, v66
	v_mov_b32_e32 v93, v66
	v_mov_b32_e32 v94, v66
	v_mov_b32_e32 v95, v66
	v_mov_b32_e32 v96, v66
	v_mov_b32_e32 v97, v66
	v_mov_b32_e32 v106, v66
	v_mov_b32_e32 v107, v66
	v_mov_b32_e32 v108, v66
	v_mov_b32_e32 v109, v66
	v_mov_b32_e32 v110, v66
	v_mov_b32_e32 v111, v66
	v_mov_b32_e32 v112, v66
	v_mov_b32_e32 v113, v66
	v_mov_b32_e32 v122, v66
	v_mov_b32_e32 v123, v66
	v_mov_b32_e32 v124, v66
	v_mov_b32_e32 v125, v66
	v_mov_b32_e32 v126, v66
	v_mov_b32_e32 v127, v66
	v_mov_b32_e32 v128, v66
	v_mov_b32_e32 v129, v66
	v_mov_b32_e32 v130, v66
	v_mov_b32_e32 v131, v66
	v_mov_b32_e32 v132, v66
	v_mov_b32_e32 v133, v66
	v_mov_b32_e32 v134, v66
	v_mov_b32_e32 v135, v66
	v_mov_b32_e32 v136, v66
	v_mov_b32_e32 v137, v66
	v_mov_b32_e32 v146, v66
	v_mov_b32_e32 v147, v66
	v_mov_b32_e32 v148, v66
	v_mov_b32_e32 v149, v66
	v_mov_b32_e32 v150, v66
	v_mov_b32_e32 v151, v66
	v_mov_b32_e32 v152, v66
	v_mov_b32_e32 v153, v66
	v_mov_b32_e32 v162, v66
	v_mov_b32_e32 v163, v66
	v_mov_b32_e32 v164, v66
	v_mov_b32_e32 v165, v66
	v_mov_b32_e32 v166, v66
	v_mov_b32_e32 v167, v66
	v_mov_b32_e32 v168, v66
	v_mov_b32_e32 v169, v66
	v_mov_b32_e32 v178, v66
	v_mov_b32_e32 v179, v66
	v_mov_b32_e32 v180, v66
	v_mov_b32_e32 v181, v66
	v_mov_b32_e32 v182, v66
	v_mov_b32_e32 v183, v66
	v_mov_b32_e32 v184, v66
	v_mov_b32_e32 v185, v66
	v_mov_b32_e32 v138, v66
	v_mov_b32_e32 v139, v66
	v_mov_b32_e32 v140, v66
	v_mov_b32_e32 v141, v66
	v_mov_b32_e32 v142, v66
	v_mov_b32_e32 v143, v66
	v_mov_b32_e32 v144, v66
	v_mov_b32_e32 v145, v66
	v_mov_b32_e32 v154, v66
	v_mov_b32_e32 v155, v66
	v_mov_b32_e32 v156, v66
	v_mov_b32_e32 v157, v66
	v_mov_b32_e32 v158, v66
	v_mov_b32_e32 v159, v66
	v_mov_b32_e32 v160, v66
	v_mov_b32_e32 v161, v66
	v_mov_b32_e32 v170, v66
	v_mov_b32_e32 v171, v66
	v_mov_b32_e32 v172, v66
	v_mov_b32_e32 v173, v66
	v_mov_b32_e32 v174, v66
	v_mov_b32_e32 v175, v66
	v_mov_b32_e32 v176, v66
	v_mov_b32_e32 v177, v66
	v_mov_b32_e32 v186, v66
	v_mov_b32_e32 v187, v66
	v_mov_b32_e32 v188, v66
	v_mov_b32_e32 v189, v66
	v_mov_b32_e32 v190, v66
	v_mov_b32_e32 v191, v66
	v_mov_b32_e32 v192, v66
	v_mov_b32_e32 v193, v66
	v_bfe_u32 v202, v0, 4, 2
	v_add_u32_e32 v203, s0, v198
	v_add_u32_e32 v204, s0, v199
	v_add_u32_e32 v205, s1, v198
	v_add_u32_e32 v206, s1, v199
	s_barrier
	s_cmpk_eq_i32 s10, 0x700
	s_cselect_b64 s[18:19], -1, 0
	s_cmpk_lg_i32 s10, 0x700
	s_cselect_b64 s[26:27], -1, 0
	s_add_u32 s54, s48, s10
	s_addc_u32 s55, s49, s11
	s_add_u32 s51, s8, s10
	s_addc_u32 s52, s25, s11
	s_add_u32 s20, s51, 0x100
	s_addc_u32 s53, s52, 0
	s_add_u32 s12, s54, 0x100080
	s_addc_u32 s0, s55, 0
	s_and_b32 s13, s0, 0xffff
	v_add_u32_e32 v210, 0x1c000, v198
	v_add_u32_e32 v211, 0x1c000, v199
	s_cmpk_lt_u32 s3, 0x100
	s_cbranch_scc0 .Lp2_prio_done
	s_setprio 1

.LBB4_12:
	s_and_b32 s33, s0, 3
	s_add_u32 s12, s8, 0x80
	s_addc_u32 s0, s3, 0
	s_add_i32 s36, s7, 0x18000
	s_and_b32 s13, s0, 0xffff
	s_mov_b32 m0, s36
	s_add_i32 s37, s7, 0x1a000
	s_waitcnt vmcnt(4)
	s_barrier
	buffer_load_dwordx4 v193, s[12:15], 0 offen lds
	s_mov_b32 m0, s37
	v_lshrrev_b32_e32 v1, 4, v0
	buffer_load_dwordx4 v195, s[12:15], 0 offen lds
	s_add_u32 s12, s16, 0x80
	s_addc_u32 s0, s9, 0
	s_add_i32 s38, s7, 0x8000
	s_and_b32 s13, s0, 0xffff
	s_mov_b32 m0, s38
	s_add_i32 s39, s7, 0xa000
	buffer_load_dwordx4 v192, s[12:15], 0 offen lds
	s_mov_b32 m0, s39
	v_and_b32_e32 v196, 15, v0
	buffer_load_dwordx4 v194, s[12:15], 0 offen lds
	s_add_u32 s12, s8, 0x4080
	s_addc_u32 s0, s3, 0
	s_add_i32 s40, s7, 0x1c000
	s_and_b32 s13, s0, 0xffff
	s_mov_b32 m0, s40
	s_add_i32 s41, s7, 0x1e000
	buffer_load_dwordx4 v193, s[12:15], 0 offen lds
	s_mov_b32 m0, s41
	v_bfe_u32 v197, v0, 4, 2
	buffer_load_dwordx4 v195, s[12:15], 0 offen lds
	v_bfe_u32 v0, v0, 1, 3
	v_bitop3_b32 v0, v1, v0, 3 bitop3:0x6c
	v_lshlrev_b32_e32 v1, 7, v196
	v_lshlrev_b32_e32 v0, 4, v0
	v_lshl_or_b32 v2, s27, 13, v1
	v_lshl_or_b32 v1, s33, 12, v1
	s_waitcnt vmcnt(6)
	v_or_b32_e32 v3, v2, v0
	v_or_b32_e32 v198, v1, v0
	v_bitop3_b32 v2, v2, 64, v0 bitop3:0x36
	v_bitop3_b32 v199, v1, 64, v0 bitop3:0x36
	v_mov_b32_e32 v64, 0
	s_add_i32 s0, 0, 0x10000
	s_add_i32 s1, 0, 0x14000
	s_add_i32 s42, s7, 0xc000
	s_add_i32 s43, s7, 0xe000
	s_mov_b32 s44, -2
	s_mov_b64 s[10:11], 0
	v_add_u32_e32 v200, 0, v3
	v_add_u32_e32 v201, 0, v2
	s_add_i32 s45, 0, 0x18000
	v_mov_b32_e32 v65, v64
	v_mov_b32_e32 v66, v64
	v_mov_b32_e32 v67, v64
	v_mov_b32_e32 v68, v64
	v_mov_b32_e32 v69, v64
	v_mov_b32_e32 v70, v64
	v_mov_b32_e32 v71, v64
	v_mov_b32_e32 v80, v64
	v_mov_b32_e32 v81, v64
	v_mov_b32_e32 v82, v64
	v_mov_b32_e32 v83, v64
	v_mov_b32_e32 v84, v64
	v_mov_b32_e32 v85, v64
	v_mov_b32_e32 v86, v64
	v_mov_b32_e32 v87, v64
	v_mov_b32_e32 v96, v64
	v_mov_b32_e32 v97, v64
	v_mov_b32_e32 v98, v64
	v_mov_b32_e32 v99, v64
	v_mov_b32_e32 v100, v64
	v_mov_b32_e32 v101, v64
	v_mov_b32_e32 v102, v64
	v_mov_b32_e32 v103, v64
	v_mov_b32_e32 v112, v64
	v_mov_b32_e32 v113, v64
	v_mov_b32_e32 v114, v64
	v_mov_b32_e32 v115, v64
	v_mov_b32_e32 v116, v64
	v_mov_b32_e32 v117, v64
	v_mov_b32_e32 v118, v64
	v_mov_b32_e32 v119, v64
	v_mov_b32_e32 v72, v64
	v_mov_b32_e32 v73, v64
	v_mov_b32_e32 v74, v64
	v_mov_b32_e32 v75, v64
	v_mov_b32_e32 v76, v64
	v_mov_b32_e32 v77, v64
	v_mov_b32_e32 v78, v64
	v_mov_b32_e32 v79, v64
	v_mov_b32_e32 v88, v64
	v_mov_b32_e32 v89, v64
	v_mov_b32_e32 v90, v64
	v_mov_b32_e32 v91, v64
	v_mov_b32_e32 v92, v64
	v_mov_b32_e32 v93, v64
	v_mov_b32_e32 v94, v64
	v_mov_b32_e32 v95, v64
	v_mov_b32_e32 v104, v64
	v_mov_b32_e32 v105, v64
	v_mov_b32_e32 v106, v64
	v_mov_b32_e32 v107, v64
	v_mov_b32_e32 v108, v64
	v_mov_b32_e32 v109, v64
	v_mov_b32_e32 v110, v64
	v_mov_b32_e32 v111, v64
	v_mov_b32_e32 v120, v64
	v_mov_b32_e32 v121, v64
	v_mov_b32_e32 v122, v64
	v_mov_b32_e32 v123, v64
	v_mov_b32_e32 v124, v64
	v_mov_b32_e32 v125, v64
	v_mov_b32_e32 v126, v64
	v_mov_b32_e32 v127, v64
	v_mov_b32_e32 v128, v64
	v_mov_b32_e32 v129, v64
	v_mov_b32_e32 v130, v64
	v_mov_b32_e32 v131, v64
	v_mov_b32_e32 v132, v64
	v_mov_b32_e32 v133, v64
	v_mov_b32_e32 v134, v64
	v_mov_b32_e32 v135, v64
	v_mov_b32_e32 v144, v64
	v_mov_b32_e32 v145, v64
	v_mov_b32_e32 v146, v64
	v_mov_b32_e32 v147, v64
	v_mov_b32_e32 v148, v64
	v_mov_b32_e32 v149, v64
	v_mov_b32_e32 v150, v64
	v_mov_b32_e32 v151, v64
	v_mov_b32_e32 v160, v64
	v_mov_b32_e32 v161, v64
	v_mov_b32_e32 v162, v64
	v_mov_b32_e32 v163, v64
	v_mov_b32_e32 v164, v64
	v_mov_b32_e32 v165, v64
	v_mov_b32_e32 v166, v64
	v_mov_b32_e32 v167, v64
	v_mov_b32_e32 v176, v64
	v_mov_b32_e32 v177, v64
	v_mov_b32_e32 v178, v64
	v_mov_b32_e32 v179, v64
	v_mov_b32_e32 v180, v64
	v_mov_b32_e32 v181, v64
	v_mov_b32_e32 v182, v64
	v_mov_b32_e32 v183, v64
	v_mov_b32_e32 v136, v64
	v_mov_b32_e32 v137, v64
	v_mov_b32_e32 v138, v64
	v_mov_b32_e32 v139, v64
	v_mov_b32_e32 v140, v64
	v_mov_b32_e32 v141, v64
	v_mov_b32_e32 v142, v64
	v_mov_b32_e32 v143, v64
	v_mov_b32_e32 v152, v64
	v_mov_b32_e32 v153, v64
	v_mov_b32_e32 v154, v64
	v_mov_b32_e32 v155, v64
	v_mov_b32_e32 v156, v64
	v_mov_b32_e32 v157, v64
	v_mov_b32_e32 v158, v64
	v_mov_b32_e32 v159, v64
	v_mov_b32_e32 v168, v64
	v_mov_b32_e32 v169, v64
	v_mov_b32_e32 v170, v64
	v_mov_b32_e32 v171, v64
	v_mov_b32_e32 v172, v64
	v_mov_b32_e32 v173, v64
	v_mov_b32_e32 v174, v64
	v_mov_b32_e32 v175, v64
	v_mov_b32_e32 v184, v64
	v_mov_b32_e32 v185, v64
	v_mov_b32_e32 v186, v64
	v_mov_b32_e32 v187, v64
	v_mov_b32_e32 v188, v64
	v_mov_b32_e32 v189, v64
	v_mov_b32_e32 v190, v64
	v_mov_b32_e32 v191, v64
	v_add_u32_e32 v202, s0, v198
	v_add_u32_e32 v203, s0, v199
	v_add_u32_e32 v204, s1, v198
	v_add_u32_e32 v205, s1, v199
	s_barrier
	s_cmpk_eq_i32 s10, 0x700
	s_cselect_b64 s[18:19], -1, 0
	s_cmpk_lg_i32 s10, 0x700
	s_cselect_b64 s[24:25], -1, 0
	s_add_u32 s49, s16, s10
	s_addc_u32 s50, s9, s11
	s_add_u32 s46, s8, s10
	s_addc_u32 s47, s3, s11
	s_add_u32 s20, s46, 0x100
	s_addc_u32 s48, s47, 0
	s_add_u32 s12, s49, 0x40080
	s_addc_u32 s0, s50, 0
	s_and_b32 s13, s0, 0xffff
	v_add_u32_e32 v207, 0x1c000, v198
	v_add_u32_e32 v208, 0x1c000, v199
	s_cmpk_lt_u32 s26, 0x100
	s_cbranch_scc0 .Lp3_prio_done
	s_setprio 1

.LBB5_16:
	s_and_b32 s35, s20, 3
	s_add_u32 s8, s12, 0x80
	s_load_dword s2, s[0:1], 0x48
	s_addc_u32 s0, s7, 0
	s_add_i32 s37, s25, 0x18000
	s_and_b32 s9, s0, 0xffff
	s_mov_b32 m0, s37
	s_add_i32 s38, s25, 0x1a000
	s_waitcnt vmcnt(4)
	s_barrier
	buffer_load_dwordx4 v192, s[8:11], 0 offen lds
	s_mov_b32 m0, s38
	v_lshrrev_b32_e32 v1, 4, v0
	buffer_load_dwordx4 v193, s[8:11], 0 offen lds
	s_add_u32 s8, s16, 0x80
	s_addc_u32 s0, s13, 0
	s_add_i32 s39, s25, 0x8000
	s_and_b32 s9, s0, 0xffff
	s_mov_b32 m0, s39
	s_add_i32 s40, s25, 0xa000
	buffer_load_dwordx4 v192, s[8:11], 0 offen lds
	s_mov_b32 m0, s40
	v_and_b32_e32 v194, 15, v0
	buffer_load_dwordx4 v193, s[8:11], 0 offen lds
	s_add_u32 s8, s12, 0x40080
	s_addc_u32 s0, s7, 0
	s_add_i32 s41, s25, 0x1c000
	s_and_b32 s9, s0, 0xffff
	s_mov_b32 m0, s41
	s_add_i32 s42, s25, 0x1e000
	buffer_load_dwordx4 v192, s[8:11], 0 offen lds
	s_mov_b32 m0, s42
	v_bfe_u32 v195, v0, 4, 2
	buffer_load_dwordx4 v193, s[8:11], 0 offen lds
	v_bfe_u32 v0, v0, 1, 3
	v_bitop3_b32 v0, v1, v0, 3 bitop3:0x6c
	v_lshlrev_b32_e32 v1, 7, v194
	v_lshlrev_b32_e32 v0, 4, v0
	v_lshl_or_b32 v2, s3, 13, v1
	v_lshl_or_b32 v1, s35, 12, v1
	s_waitcnt vmcnt(6)
	v_or_b32_e32 v3, v2, v0
	v_or_b32_e32 v196, v1, v0
	v_bitop3_b32 v2, v2, 64, v0 bitop3:0x36
	v_bitop3_b32 v197, v1, 64, v0 bitop3:0x36
	v_mov_b32_e32 v64, 0
	s_add_i32 s0, 0, 0x10000
	s_add_i32 s1, 0, 0x14000
	s_add_i32 s43, s25, 0xc000
	s_add_i32 s44, s25, 0xe000
	s_mov_b32 s45, -2
	s_mov_b64 s[14:15], 0
	v_add_u32_e32 v198, 0, v3
	v_add_u32_e32 v199, 0, v2
	s_add_i32 s46, 0, 0x18000
	v_mov_b32_e32 v65, v64
	v_mov_b32_e32 v66, v64
	v_mov_b32_e32 v67, v64
	v_mov_b32_e32 v68, v64
	v_mov_b32_e32 v69, v64
	v_mov_b32_e32 v70, v64
	v_mov_b32_e32 v71, v64
	v_mov_b32_e32 v76, v64
	v_mov_b32_e32 v77, v64
	v_mov_b32_e32 v78, v64
	v_mov_b32_e32 v79, v64
	v_mov_b32_e32 v80, v64
	v_mov_b32_e32 v81, v64
	v_mov_b32_e32 v82, v64
	v_mov_b32_e32 v83, v64
	v_mov_b32_e32 v88, v64
	v_mov_b32_e32 v89, v64
	v_mov_b32_e32 v90, v64
	v_mov_b32_e32 v91, v64
	v_mov_b32_e32 v92, v64
	v_mov_b32_e32 v93, v64
	v_mov_b32_e32 v94, v64
	v_mov_b32_e32 v95, v64
	v_mov_b32_e32 v104, v64
	v_mov_b32_e32 v105, v64
	v_mov_b32_e32 v106, v64
	v_mov_b32_e32 v107, v64
	v_mov_b32_e32 v108, v64
	v_mov_b32_e32 v109, v64
	v_mov_b32_e32 v110, v64
	v_mov_b32_e32 v111, v64
	v_mov_b32_e32 v72, v64
	v_mov_b32_e32 v73, v64
	v_mov_b32_e32 v74, v64
	v_mov_b32_e32 v75, v64
	v_mov_b32_e32 v84, v64
	v_mov_b32_e32 v85, v64
	v_mov_b32_e32 v86, v64
	v_mov_b32_e32 v87, v64
	v_mov_b32_e32 v96, v64
	v_mov_b32_e32 v97, v64
	v_mov_b32_e32 v98, v64
	v_mov_b32_e32 v99, v64
	v_mov_b32_e32 v100, v64
	v_mov_b32_e32 v101, v64
	v_mov_b32_e32 v102, v64
	v_mov_b32_e32 v103, v64
	v_mov_b32_e32 v112, v64
	v_mov_b32_e32 v113, v64
	v_mov_b32_e32 v114, v64
	v_mov_b32_e32 v115, v64
	v_mov_b32_e32 v116, v64
	v_mov_b32_e32 v117, v64
	v_mov_b32_e32 v118, v64
	v_mov_b32_e32 v119, v64
	v_mov_b32_e32 v120, v64
	v_mov_b32_e32 v121, v64
	v_mov_b32_e32 v122, v64
	v_mov_b32_e32 v123, v64
	v_mov_b32_e32 v124, v64
	v_mov_b32_e32 v125, v64
	v_mov_b32_e32 v126, v64
	v_mov_b32_e32 v127, v64
	v_mov_b32_e32 v128, v64
	v_mov_b32_e32 v129, v64
	v_mov_b32_e32 v130, v64
	v_mov_b32_e32 v131, v64
	v_mov_b32_e32 v132, v64
	v_mov_b32_e32 v133, v64
	v_mov_b32_e32 v134, v64
	v_mov_b32_e32 v135, v64
	v_mov_b32_e32 v140, v64
	v_mov_b32_e32 v141, v64
	v_mov_b32_e32 v142, v64
	v_mov_b32_e32 v143, v64
	v_mov_b32_e32 v148, v64
	v_mov_b32_e32 v149, v64
	v_mov_b32_e32 v150, v64
	v_mov_b32_e32 v151, v64
	v_mov_b32_e32 v156, v64
	v_mov_b32_e32 v157, v64
	v_mov_b32_e32 v158, v64
	v_mov_b32_e32 v159, v64
	v_mov_b32_e32 v164, v64
	v_mov_b32_e32 v165, v64
	v_mov_b32_e32 v166, v64
	v_mov_b32_e32 v167, v64
	v_mov_b32_e32 v172, v64
	v_mov_b32_e32 v173, v64
	v_mov_b32_e32 v174, v64
	v_mov_b32_e32 v175, v64
	v_mov_b32_e32 v180, v64
	v_mov_b32_e32 v181, v64
	v_mov_b32_e32 v182, v64
	v_mov_b32_e32 v183, v64
	v_mov_b32_e32 v136, v64
	v_mov_b32_e32 v137, v64
	v_mov_b32_e32 v138, v64
	v_mov_b32_e32 v139, v64
	v_mov_b32_e32 v144, v64
	v_mov_b32_e32 v145, v64
	v_mov_b32_e32 v146, v64
	v_mov_b32_e32 v147, v64
	v_mov_b32_e32 v152, v64
	v_mov_b32_e32 v153, v64
	v_mov_b32_e32 v154, v64
	v_mov_b32_e32 v155, v64
	v_mov_b32_e32 v160, v64
	v_mov_b32_e32 v161, v64
	v_mov_b32_e32 v162, v64
	v_mov_b32_e32 v163, v64
	v_mov_b32_e32 v168, v64
	v_mov_b32_e32 v169, v64
	v_mov_b32_e32 v170, v64
	v_mov_b32_e32 v171, v64
	v_mov_b32_e32 v176, v64
	v_mov_b32_e32 v177, v64
	v_mov_b32_e32 v178, v64
	v_mov_b32_e32 v179, v64
	v_mov_b32_e32 v184, v64
	v_mov_b32_e32 v185, v64
	v_mov_b32_e32 v186, v64
	v_mov_b32_e32 v187, v64
	v_mov_b32_e32 v188, v64
	v_mov_b32_e32 v189, v64
	v_mov_b32_e32 v190, v64
	v_mov_b32_e32 v191, v64
	v_add_u32_e32 v200, s0, v196
	v_add_u32_e32 v201, s0, v197
	v_add_u32_e32 v202, s1, v196
	v_add_u32_e32 v203, s1, v197
	s_barrier
	s_cmpk_eq_i32 s14, 0x700
	s_cselect_b64 s[18:19], -1, 0
	s_cmpk_lg_i32 s14, 0x700
	s_cselect_b64 s[26:27], -1, 0
	s_add_u32 s50, s16, s14
	s_addc_u32 s51, s13, s15
	s_add_u32 s47, s12, s14
	s_addc_u32 s48, s7, s15
	s_add_u32 s20, s47, 0x100
	s_addc_u32 s49, s48, 0
	s_add_u32 s8, s50, 0x40080
	s_addc_u32 s0, s51, 0
	s_and_b32 s9, s0, 0xffff
	v_add_u32_e32 v205, 0x1c000, v196
	v_add_u32_e32 v206, 0x1c000, v197
	s_cmpk_lt_u32 s28, 0x100
	s_cbranch_scc0 .Lp4_prio_done
	s_setprio 1
